# v18 plus non-temporal (nt) hint on the P11 and P4 epilogue output stores
# baseline (speedup 1.0000x reference)
.LBB0_759:
	s_lshl_b32 s15, s57, 11
	v_mov_b32_e32 v196, v198
	s_and_b32 s15, s15, 0x800
	s_add_i32 s15, s52, s15
	v_and_b32_e32 v210, 15, v196
	v_lshl_add_u32 v211, v210, 3, s15
	ds_read2_b64 v[192:195], v211 offset1:16
	v_ashrrev_i32_e32 v214, 1, v196
	s_lshl_b32 s15, s22, 8
	s_add_i32 s15, s15, s50
	v_or_b32_e32 v210, s15, v210
	s_waitcnt lgkmcnt(0)
	v_mov_b32_e32 v196, v193
	v_lshlrev_b64 v[212:213], s54, v[196:197]
	v_min_u32_e32 v193, 1, v212
	v_or_b32_e32 v193, v213, v193
	v_cvt_f32_u32_e32 v193, v193
	v_cvt_f32_u32_e32 v192, v192
	s_sub_i32 s15, 32, s54
	v_mov_b32_e32 v196, v195
	v_ldexp_f32 v193, v193, s15
	v_fmamk_f32 v212, v192, 0x2e000000, v209
	v_fmac_f32_e32 v212, 0x3e000000, v193
	v_lshlrev_b64 v[192:193], s54, v[196:197]
	v_min_u32_e32 v192, 1, v192
	v_or_b32_e32 v192, v193, v192
	v_cvt_f32_u32_e32 v196, v192
	v_cvt_f32_u32_e32 v213, v194
	ds_read2_b64 v[192:195], v211 offset0:32 offset1:48
	v_rsq_f32_e32 v215, v212
	v_ldexp_f32 v196, v196, s15
	v_fmamk_f32 v212, v213, 0x2e000000, v209
	v_fmac_f32_e32 v212, 0x3e000000, v196
	s_waitcnt lgkmcnt(0)
	v_mov_b32_e32 v196, v193
	v_rsq_f32_e32 v216, v212
	v_lshlrev_b64 v[212:213], s54, v[196:197]
	v_min_u32_e32 v193, 1, v212
	v_or_b32_e32 v193, v213, v193
	v_cvt_f32_u32_e32 v193, v193
	v_cvt_f32_u32_e32 v192, v192
	v_mov_b32_e32 v196, v195
	v_cvt_f32_u32_e32 v213, v194
	v_ldexp_f32 v193, v193, s15
	v_fmamk_f32 v212, v192, 0x2e000000, v209
	v_fmac_f32_e32 v212, 0x3e000000, v193
	v_lshlrev_b64 v[192:193], s54, v[196:197]
	v_min_u32_e32 v192, 1, v192
	v_or_b32_e32 v192, v193, v192
	v_cvt_f32_u32_e32 v196, v192
	ds_read2_b64 v[192:195], v211 offset0:128 offset1:144
	v_rsq_f32_e32 v217, v212
	v_fmamk_f32 v212, v213, 0x2e000000, v209
	v_ldexp_f32 v196, v196, s15
	v_fmac_f32_e32 v212, 0x3e000000, v196
	s_waitcnt lgkmcnt(0)
	v_mov_b32_e32 v196, v193
	v_rsq_f32_e32 v218, v212
	v_lshlrev_b64 v[212:213], s54, v[196:197]
	v_min_u32_e32 v193, 1, v212
	v_or_b32_e32 v193, v213, v193
	v_cvt_f32_u32_e32 v193, v193
	v_cvt_f32_u32_e32 v192, v192
	v_mov_b32_e32 v196, v195
	v_cvt_f32_u32_e32 v219, v194
	v_ldexp_f32 v212, v193, s15
	v_fmamk_f32 v213, v192, 0x2e000000, v209
	v_lshlrev_b64 v[192:193], s54, v[196:197]
	v_min_u32_e32 v192, 1, v192
	v_or_b32_e32 v192, v193, v192
	v_cvt_f32_u32_e32 v196, v192
	ds_read2_b64 v[192:195], v211 offset0:160 offset1:176
	v_fmac_f32_e32 v213, 0x3e000000, v212
	v_rsq_f32_e32 v211, v213
	v_ldexp_f32 v220, v196, s15
	v_fmamk_f32 v219, v219, 0x2e000000, v209
	s_waitcnt lgkmcnt(0)
	v_mov_b32_e32 v196, v193
	v_lshlrev_b64 v[212:213], s54, v[196:197]
	v_min_u32_e32 v193, 1, v212
	v_or_b32_e32 v193, v213, v193
	v_cvt_f32_u32_e32 v193, v193
	v_cvt_f32_u32_e32 v192, v192
	v_fmac_f32_e32 v219, 0x3e000000, v220
	v_mov_b32_e32 v196, v195
	v_rsq_f32_e32 v212, v219
	v_ldexp_f32 v213, v193, s15
	v_fmamk_f32 v219, v192, 0x2e000000, v209
	v_lshlrev_b64 v[192:193], s54, v[196:197]
	v_min_u32_e32 v192, 1, v192
	v_or_b32_e32 v192, v193, v192
	v_cvt_f32_u32_e32 v192, v192
	v_cvt_f32_u32_e32 v193, v194
	v_fmac_f32_e32 v219, 0x3e000000, v213
	v_rsq_f32_e32 v194, v219
	v_ldexp_f32 v192, v192, s15
	v_fmamk_f32 v193, v193, 0x2e000000, v209
	v_fmac_f32_e32 v193, 0x3e000000, v192
	v_rsq_f32_e32 v192, v193
	v_mul_f32_e32 v224, 0x37d834f1, v215
	v_mul_f32_e32 v225, 0x37d834f1, v216
	v_mul_f32_e32 v226, 0x37d834f1, v217
	v_mul_f32_e32 v227, 0x37d834f1, v218
	v_mul_f32_e32 v228, 0x37d834f1, v211
	v_mul_f32_e32 v229, 0x37d834f1, v212
	v_mul_f32_e32 v230, 0x37d834f1, v194
	v_mul_f32_e32 v231, 0x37d834f1, v192
	s_lshl_b32 s15, s56, 7
	v_and_b32_e32 v214, -8, v214
	s_or_b32 s15, s15, s51
	v_add_u32_e32 v214, s15, v214
	v_lshlrev_b32_e32 v214, 1, v214
	v_mad_u32_u24 v232, v210, s53, v214
	v_mul_f32_e32 v78, 0xbfb8aa3b, v224
	v_mul_f32_e32 v20, v224, v224
	v_rcp_f32_e32 v20, v20
	v_cvt_f32_i32_e32 v184, v184
	v_cvt_f32_i32_e32 v185, v185
	v_cvt_f32_i32_e32 v186, v186
	v_cvt_f32_i32_e32 v187, v187
	v_cvt_f32_i32_e32 v176, v176
	v_cvt_f32_i32_e32 v177, v177
	v_cvt_f32_i32_e32 v178, v178
	v_cvt_f32_i32_e32 v179, v179
	v_cvt_f32_i32_e32 v188, v188
	v_cvt_f32_i32_e32 v189, v189
	v_cvt_f32_i32_e32 v190, v190
	v_cvt_f32_i32_e32 v191, v191
	v_cvt_f32_i32_e32 v180, v180
	v_cvt_f32_i32_e32 v181, v181
	v_cvt_f32_i32_e32 v182, v182
	v_cvt_f32_i32_e32 v183, v183
	v_pk_mul_f32 v[64:65], v[184:185], v[78:79] op_sel_hi:[1,0]
	v_pk_mul_f32 v[66:67], v[186:187], v[78:79] op_sel_hi:[1,0]
	v_pk_mul_f32 v[68:69], v[176:177], v[78:79] op_sel_hi:[1,0]
	v_pk_mul_f32 v[70:71], v[178:179], v[78:79] op_sel_hi:[1,0]
	v_exp_f32_e32 v64, v64
	v_exp_f32_e32 v65, v65
	v_exp_f32_e32 v66, v66
	v_exp_f32_e32 v67, v67
	v_exp_f32_e32 v68, v68
	v_exp_f32_e32 v69, v69
	v_exp_f32_e32 v70, v70
	v_exp_f32_e32 v71, v71
	v_pk_mul_f32 v[184:185], v[188:189], v[184:185]
	v_pk_mul_f32 v[186:187], v[190:191], v[186:187]
	v_pk_mul_f32 v[176:177], v[180:181], v[176:177]
	v_pk_mul_f32 v[178:179], v[182:183], v[178:179]
	v_pk_fma_f32 v[64:65], v[64:65], v[20:21], v[20:21] op_sel_hi:[1,0,0]
	v_pk_fma_f32 v[66:67], v[66:67], v[20:21], v[20:21] op_sel_hi:[1,0,0]
	v_pk_fma_f32 v[68:69], v[68:69], v[20:21], v[20:21] op_sel_hi:[1,0,0]
	v_pk_fma_f32 v[70:71], v[70:71], v[20:21], v[20:21] op_sel_hi:[1,0,0]
	v_rcp_f32_e32 v64, v64
	v_rcp_f32_e32 v65, v65
	v_rcp_f32_e32 v66, v66
	v_rcp_f32_e32 v67, v67
	v_rcp_f32_e32 v68, v68
	v_rcp_f32_e32 v69, v69
	v_rcp_f32_e32 v70, v70
	v_rcp_f32_e32 v71, v71
	v_mov_b32_e32 v76, v232
	v_pk_mul_f32 v[184:185], v[184:185], v[64:65]
	v_pk_mul_f32 v[186:187], v[186:187], v[66:67]
	v_pk_mul_f32 v[176:177], v[176:177], v[68:69]
	v_pk_mul_f32 v[178:179], v[178:179], v[70:71]
	v_cvt_pk_bf16_f32 v72, v184, v185
	v_cvt_pk_bf16_f32 v73, v186, v187
	v_cvt_pk_bf16_f32 v74, v176, v177
	v_cvt_pk_bf16_f32 v75, v178, v179
	global_store_dwordx4 v76, v[72:75], s[8:9] nt
	v_mul_f32_e32 v94, 0xbfb8aa3b, v225
	v_mul_f32_e32 v24, v225, v225
	v_rcp_f32_e32 v24, v24
	v_cvt_f32_i32_e32 v168, v168
	v_cvt_f32_i32_e32 v169, v169
	v_cvt_f32_i32_e32 v170, v170
	v_cvt_f32_i32_e32 v171, v171
	v_cvt_f32_i32_e32 v160, v160
	v_cvt_f32_i32_e32 v161, v161
	v_cvt_f32_i32_e32 v162, v162
	v_cvt_f32_i32_e32 v163, v163
	v_cvt_f32_i32_e32 v172, v172
	v_cvt_f32_i32_e32 v173, v173
	v_cvt_f32_i32_e32 v174, v174
	v_cvt_f32_i32_e32 v175, v175
	v_cvt_f32_i32_e32 v164, v164
	v_cvt_f32_i32_e32 v165, v165
	v_cvt_f32_i32_e32 v166, v166
	v_cvt_f32_i32_e32 v167, v167
	v_pk_mul_f32 v[80:81], v[168:169], v[94:95] op_sel_hi:[1,0]
	v_pk_mul_f32 v[82:83], v[170:171], v[94:95] op_sel_hi:[1,0]
	v_pk_mul_f32 v[84:85], v[160:161], v[94:95] op_sel_hi:[1,0]
	v_pk_mul_f32 v[86:87], v[162:163], v[94:95] op_sel_hi:[1,0]
	v_exp_f32_e32 v80, v80
	v_exp_f32_e32 v81, v81
	v_exp_f32_e32 v82, v82
	v_exp_f32_e32 v83, v83
	v_exp_f32_e32 v84, v84
	v_exp_f32_e32 v85, v85
	v_exp_f32_e32 v86, v86
	v_exp_f32_e32 v87, v87
	v_pk_mul_f32 v[168:169], v[172:173], v[168:169]
	v_pk_mul_f32 v[170:171], v[174:175], v[170:171]
	v_pk_mul_f32 v[160:161], v[164:165], v[160:161]
	v_pk_mul_f32 v[162:163], v[166:167], v[162:163]
	v_pk_fma_f32 v[80:81], v[80:81], v[24:25], v[24:25] op_sel_hi:[1,0,0]
	v_pk_fma_f32 v[82:83], v[82:83], v[24:25], v[24:25] op_sel_hi:[1,0,0]
	v_pk_fma_f32 v[84:85], v[84:85], v[24:25], v[24:25] op_sel_hi:[1,0,0]
	v_pk_fma_f32 v[86:87], v[86:87], v[24:25], v[24:25] op_sel_hi:[1,0,0]
	v_rcp_f32_e32 v80, v80
	v_rcp_f32_e32 v81, v81
	v_rcp_f32_e32 v82, v82
	v_rcp_f32_e32 v83, v83
	v_rcp_f32_e32 v84, v84
	v_rcp_f32_e32 v85, v85
	v_rcp_f32_e32 v86, v86
	v_rcp_f32_e32 v87, v87
	v_add_u32_e32 v92, 0x2c000, v232
	v_pk_mul_f32 v[168:169], v[168:169], v[80:81]
	v_pk_mul_f32 v[170:171], v[170:171], v[82:83]
	v_pk_mul_f32 v[160:161], v[160:161], v[84:85]
	v_pk_mul_f32 v[162:163], v[162:163], v[86:87]
	v_cvt_pk_bf16_f32 v88, v168, v169
	v_cvt_pk_bf16_f32 v89, v170, v171
	v_cvt_pk_bf16_f32 v90, v160, v161
	v_cvt_pk_bf16_f32 v91, v162, v163
	global_store_dwordx4 v92, v[88:91], s[8:9] nt
	v_mul_f32_e32 v78, 0xbfb8aa3b, v226
	v_mul_f32_e32 v20, v226, v226
	v_rcp_f32_e32 v20, v20
	v_cvt_f32_i32_e32 v152, v152
	v_cvt_f32_i32_e32 v153, v153
	v_cvt_f32_i32_e32 v154, v154
	v_cvt_f32_i32_e32 v155, v155
	v_cvt_f32_i32_e32 v144, v144
	v_cvt_f32_i32_e32 v145, v145
	v_cvt_f32_i32_e32 v146, v146
	v_cvt_f32_i32_e32 v147, v147
	v_cvt_f32_i32_e32 v156, v156
	v_cvt_f32_i32_e32 v157, v157
	v_cvt_f32_i32_e32 v158, v158
	v_cvt_f32_i32_e32 v159, v159
	v_cvt_f32_i32_e32 v148, v148
	v_cvt_f32_i32_e32 v149, v149
	v_cvt_f32_i32_e32 v150, v150
	v_cvt_f32_i32_e32 v151, v151
	v_pk_mul_f32 v[64:65], v[152:153], v[78:79] op_sel_hi:[1,0]
	v_pk_mul_f32 v[66:67], v[154:155], v[78:79] op_sel_hi:[1,0]
	v_pk_mul_f32 v[68:69], v[144:145], v[78:79] op_sel_hi:[1,0]
	v_pk_mul_f32 v[70:71], v[146:147], v[78:79] op_sel_hi:[1,0]
	v_exp_f32_e32 v64, v64
	v_exp_f32_e32 v65, v65
	v_exp_f32_e32 v66, v66
	v_exp_f32_e32 v67, v67
	v_exp_f32_e32 v68, v68
	v_exp_f32_e32 v69, v69
	v_exp_f32_e32 v70, v70
	v_exp_f32_e32 v71, v71
	v_pk_mul_f32 v[152:153], v[156:157], v[152:153]
	v_pk_mul_f32 v[154:155], v[158:159], v[154:155]
	v_pk_mul_f32 v[144:145], v[148:149], v[144:145]
	v_pk_mul_f32 v[146:147], v[150:151], v[146:147]
	v_pk_fma_f32 v[64:65], v[64:65], v[20:21], v[20:21] op_sel_hi:[1,0,0]
	v_pk_fma_f32 v[66:67], v[66:67], v[20:21], v[20:21] op_sel_hi:[1,0,0]
	v_pk_fma_f32 v[68:69], v[68:69], v[20:21], v[20:21] op_sel_hi:[1,0,0]
	v_pk_fma_f32 v[70:71], v[70:71], v[20:21], v[20:21] op_sel_hi:[1,0,0]
	v_rcp_f32_e32 v64, v64
	v_rcp_f32_e32 v65, v65
	v_rcp_f32_e32 v66, v66
	v_rcp_f32_e32 v67, v67
	v_rcp_f32_e32 v68, v68
	v_rcp_f32_e32 v69, v69
	v_rcp_f32_e32 v70, v70
	v_rcp_f32_e32 v71, v71
	v_add_u32_e32 v76, 0x58000, v232
	v_pk_mul_f32 v[152:153], v[152:153], v[64:65]
	v_pk_mul_f32 v[154:155], v[154:155], v[66:67]
	v_pk_mul_f32 v[144:145], v[144:145], v[68:69]
	v_pk_mul_f32 v[146:147], v[146:147], v[70:71]
	v_cvt_pk_bf16_f32 v72, v152, v153
	v_cvt_pk_bf16_f32 v73, v154, v155
	v_cvt_pk_bf16_f32 v74, v144, v145
	v_cvt_pk_bf16_f32 v75, v146, v147
	global_store_dwordx4 v76, v[72:75], s[8:9] nt
	v_mul_f32_e32 v94, 0xbfb8aa3b, v227
	v_mul_f32_e32 v24, v227, v227
	v_rcp_f32_e32 v24, v24
	v_cvt_f32_i32_e32 v136, v136
	v_cvt_f32_i32_e32 v137, v137
	v_cvt_f32_i32_e32 v138, v138
	v_cvt_f32_i32_e32 v139, v139
	v_cvt_f32_i32_e32 v128, v128
	v_cvt_f32_i32_e32 v129, v129
	v_cvt_f32_i32_e32 v130, v130
	v_cvt_f32_i32_e32 v131, v131
	v_cvt_f32_i32_e32 v140, v140
	v_cvt_f32_i32_e32 v141, v141
	v_cvt_f32_i32_e32 v142, v142
	v_cvt_f32_i32_e32 v143, v143
	v_cvt_f32_i32_e32 v132, v132
	v_cvt_f32_i32_e32 v133, v133
	v_cvt_f32_i32_e32 v134, v134
	v_cvt_f32_i32_e32 v135, v135
	v_pk_mul_f32 v[80:81], v[136:137], v[94:95] op_sel_hi:[1,0]
	v_pk_mul_f32 v[82:83], v[138:139], v[94:95] op_sel_hi:[1,0]
	v_pk_mul_f32 v[84:85], v[128:129], v[94:95] op_sel_hi:[1,0]
	v_pk_mul_f32 v[86:87], v[130:131], v[94:95] op_sel_hi:[1,0]
	v_exp_f32_e32 v80, v80
	v_exp_f32_e32 v81, v81
	v_exp_f32_e32 v82, v82
	v_exp_f32_e32 v83, v83
	v_exp_f32_e32 v84, v84
	v_exp_f32_e32 v85, v85
	v_exp_f32_e32 v86, v86
	v_exp_f32_e32 v87, v87
	v_pk_mul_f32 v[136:137], v[140:141], v[136:137]
	v_pk_mul_f32 v[138:139], v[142:143], v[138:139]
	v_pk_mul_f32 v[128:129], v[132:133], v[128:129]
	v_pk_mul_f32 v[130:131], v[134:135], v[130:131]
	v_pk_fma_f32 v[80:81], v[80:81], v[24:25], v[24:25] op_sel_hi:[1,0,0]
	v_pk_fma_f32 v[82:83], v[82:83], v[24:25], v[24:25] op_sel_hi:[1,0,0]
	v_pk_fma_f32 v[84:85], v[84:85], v[24:25], v[24:25] op_sel_hi:[1,0,0]
	v_pk_fma_f32 v[86:87], v[86:87], v[24:25], v[24:25] op_sel_hi:[1,0,0]
	v_rcp_f32_e32 v80, v80
	v_rcp_f32_e32 v81, v81
	v_rcp_f32_e32 v82, v82
	v_rcp_f32_e32 v83, v83
	v_rcp_f32_e32 v84, v84
	v_rcp_f32_e32 v85, v85
	v_rcp_f32_e32 v86, v86
	v_rcp_f32_e32 v87, v87
	v_add_u32_e32 v92, 0x84000, v232
	v_pk_mul_f32 v[136:137], v[136:137], v[80:81]
	v_pk_mul_f32 v[138:139], v[138:139], v[82:83]
	v_pk_mul_f32 v[128:129], v[128:129], v[84:85]
	v_pk_mul_f32 v[130:131], v[130:131], v[86:87]
	v_cvt_pk_bf16_f32 v88, v136, v137
	v_cvt_pk_bf16_f32 v89, v138, v139
	v_cvt_pk_bf16_f32 v90, v128, v129
	v_cvt_pk_bf16_f32 v91, v130, v131
	global_store_dwordx4 v92, v[88:91], s[8:9] nt
	v_mul_f32_e32 v78, 0xbfb8aa3b, v228
	v_mul_f32_e32 v20, v228, v228
	v_rcp_f32_e32 v20, v20
	v_cvt_f32_i32_e32 v120, v120
	v_cvt_f32_i32_e32 v121, v121
	v_cvt_f32_i32_e32 v122, v122
	v_cvt_f32_i32_e32 v123, v123
	v_cvt_f32_i32_e32 v112, v112
	v_cvt_f32_i32_e32 v113, v113
	v_cvt_f32_i32_e32 v114, v114
	v_cvt_f32_i32_e32 v115, v115
	v_cvt_f32_i32_e32 v124, v124
	v_cvt_f32_i32_e32 v125, v125
	v_cvt_f32_i32_e32 v126, v126
	v_cvt_f32_i32_e32 v127, v127
	v_cvt_f32_i32_e32 v116, v116
	v_cvt_f32_i32_e32 v117, v117
	v_cvt_f32_i32_e32 v118, v118
	v_cvt_f32_i32_e32 v119, v119
	v_pk_mul_f32 v[64:65], v[120:121], v[78:79] op_sel_hi:[1,0]
	v_pk_mul_f32 v[66:67], v[122:123], v[78:79] op_sel_hi:[1,0]
	v_pk_mul_f32 v[68:69], v[112:113], v[78:79] op_sel_hi:[1,0]
	v_pk_mul_f32 v[70:71], v[114:115], v[78:79] op_sel_hi:[1,0]
	v_exp_f32_e32 v64, v64
	v_exp_f32_e32 v65, v65
	v_exp_f32_e32 v66, v66
	v_exp_f32_e32 v67, v67
	v_exp_f32_e32 v68, v68
	v_exp_f32_e32 v69, v69
	v_exp_f32_e32 v70, v70
	v_exp_f32_e32 v71, v71
	v_pk_mul_f32 v[120:121], v[124:125], v[120:121]
	v_pk_mul_f32 v[122:123], v[126:127], v[122:123]
	v_pk_mul_f32 v[112:113], v[116:117], v[112:113]
	v_pk_mul_f32 v[114:115], v[118:119], v[114:115]
	v_pk_fma_f32 v[64:65], v[64:65], v[20:21], v[20:21] op_sel_hi:[1,0,0]
	v_pk_fma_f32 v[66:67], v[66:67], v[20:21], v[20:21] op_sel_hi:[1,0,0]
	v_pk_fma_f32 v[68:69], v[68:69], v[20:21], v[20:21] op_sel_hi:[1,0,0]
	v_pk_fma_f32 v[70:71], v[70:71], v[20:21], v[20:21] op_sel_hi:[1,0,0]
	v_rcp_f32_e32 v64, v64
	v_rcp_f32_e32 v65, v65
	v_rcp_f32_e32 v66, v66
	v_rcp_f32_e32 v67, v67
	v_rcp_f32_e32 v68, v68
	v_rcp_f32_e32 v69, v69
	v_rcp_f32_e32 v70, v70
	v_rcp_f32_e32 v71, v71
	v_add_u32_e32 v76, 0x160000, v232
	v_pk_mul_f32 v[120:121], v[120:121], v[64:65]
	v_pk_mul_f32 v[122:123], v[122:123], v[66:67]
	v_pk_mul_f32 v[112:113], v[112:113], v[68:69]
	v_pk_mul_f32 v[114:115], v[114:115], v[70:71]
	v_cvt_pk_bf16_f32 v72, v120, v121
	v_cvt_pk_bf16_f32 v73, v122, v123
	v_cvt_pk_bf16_f32 v74, v112, v113
	v_cvt_pk_bf16_f32 v75, v114, v115
	global_store_dwordx4 v76, v[72:75], s[8:9] nt
	v_mul_f32_e32 v94, 0xbfb8aa3b, v229
	v_mul_f32_e32 v24, v229, v229
	v_rcp_f32_e32 v24, v24
	v_cvt_f32_i32_e32 v104, v104
	v_cvt_f32_i32_e32 v105, v105
	v_cvt_f32_i32_e32 v106, v106
	v_cvt_f32_i32_e32 v107, v107
	v_cvt_f32_i32_e32 v96, v96
	v_cvt_f32_i32_e32 v97, v97
	v_cvt_f32_i32_e32 v98, v98
	v_cvt_f32_i32_e32 v99, v99
	v_cvt_f32_i32_e32 v108, v108
	v_cvt_f32_i32_e32 v109, v109
	v_cvt_f32_i32_e32 v110, v110
	v_cvt_f32_i32_e32 v111, v111
	v_cvt_f32_i32_e32 v100, v100
	v_cvt_f32_i32_e32 v101, v101
	v_cvt_f32_i32_e32 v102, v102
	v_cvt_f32_i32_e32 v103, v103
	v_pk_mul_f32 v[80:81], v[104:105], v[94:95] op_sel_hi:[1,0]
	v_pk_mul_f32 v[82:83], v[106:107], v[94:95] op_sel_hi:[1,0]
	v_pk_mul_f32 v[84:85], v[96:97], v[94:95] op_sel_hi:[1,0]
	v_pk_mul_f32 v[86:87], v[98:99], v[94:95] op_sel_hi:[1,0]
	v_exp_f32_e32 v80, v80
	v_exp_f32_e32 v81, v81
	v_exp_f32_e32 v82, v82
	v_exp_f32_e32 v83, v83
	v_exp_f32_e32 v84, v84
	v_exp_f32_e32 v85, v85
	v_exp_f32_e32 v86, v86
	v_exp_f32_e32 v87, v87
	v_pk_mul_f32 v[104:105], v[108:109], v[104:105]
	v_pk_mul_f32 v[106:107], v[110:111], v[106:107]
	v_pk_mul_f32 v[96:97], v[100:101], v[96:97]
	v_pk_mul_f32 v[98:99], v[102:103], v[98:99]
	v_pk_fma_f32 v[80:81], v[80:81], v[24:25], v[24:25] op_sel_hi:[1,0,0]
	v_pk_fma_f32 v[82:83], v[82:83], v[24:25], v[24:25] op_sel_hi:[1,0,0]
	v_pk_fma_f32 v[84:85], v[84:85], v[24:25], v[24:25] op_sel_hi:[1,0,0]
	v_pk_fma_f32 v[86:87], v[86:87], v[24:25], v[24:25] op_sel_hi:[1,0,0]
	v_rcp_f32_e32 v80, v80
	v_rcp_f32_e32 v81, v81
	v_rcp_f32_e32 v82, v82
	v_rcp_f32_e32 v83, v83
	v_rcp_f32_e32 v84, v84
	v_rcp_f32_e32 v85, v85
	v_rcp_f32_e32 v86, v86
	v_rcp_f32_e32 v87, v87
	v_add_u32_e32 v92, 0x18c000, v232
	v_pk_mul_f32 v[104:105], v[104:105], v[80:81]
	v_pk_mul_f32 v[106:107], v[106:107], v[82:83]
	v_pk_mul_f32 v[96:97], v[96:97], v[84:85]
	v_pk_mul_f32 v[98:99], v[98:99], v[86:87]
	v_cvt_pk_bf16_f32 v88, v104, v105
	v_cvt_pk_bf16_f32 v89, v106, v107
	v_cvt_pk_bf16_f32 v90, v96, v97
	v_cvt_pk_bf16_f32 v91, v98, v99
	global_store_dwordx4 v92, v[88:91], s[8:9] nt
	v_mul_f32_e32 v78, 0xbfb8aa3b, v230
	v_mul_f32_e32 v20, v230, v230
	v_rcp_f32_e32 v20, v20
	v_cvt_f32_i32_e32 v48, v48
	v_cvt_f32_i32_e32 v49, v49
	v_cvt_f32_i32_e32 v50, v50
	v_cvt_f32_i32_e32 v51, v51
	v_cvt_f32_i32_e32 v16, v16
	v_cvt_f32_i32_e32 v17, v17
	v_cvt_f32_i32_e32 v18, v18
	v_cvt_f32_i32_e32 v19, v19
	v_cvt_f32_i32_e32 v60, v60
	v_cvt_f32_i32_e32 v61, v61
	v_cvt_f32_i32_e32 v62, v62
	v_cvt_f32_i32_e32 v63, v63
	v_cvt_f32_i32_e32 v44, v44
	v_cvt_f32_i32_e32 v45, v45
	v_cvt_f32_i32_e32 v46, v46
	v_cvt_f32_i32_e32 v47, v47
	v_pk_mul_f32 v[64:65], v[48:49], v[78:79] op_sel_hi:[1,0]
	v_pk_mul_f32 v[66:67], v[50:51], v[78:79] op_sel_hi:[1,0]
	v_pk_mul_f32 v[68:69], v[16:17], v[78:79] op_sel_hi:[1,0]
	v_pk_mul_f32 v[70:71], v[18:19], v[78:79] op_sel_hi:[1,0]
	v_exp_f32_e32 v64, v64
	v_exp_f32_e32 v65, v65
	v_exp_f32_e32 v66, v66
	v_exp_f32_e32 v67, v67
	v_exp_f32_e32 v68, v68
	v_exp_f32_e32 v69, v69
	v_exp_f32_e32 v70, v70
	v_exp_f32_e32 v71, v71
	v_pk_mul_f32 v[48:49], v[60:61], v[48:49]
	v_pk_mul_f32 v[50:51], v[62:63], v[50:51]
	v_pk_mul_f32 v[16:17], v[44:45], v[16:17]
	v_pk_mul_f32 v[18:19], v[46:47], v[18:19]
	v_pk_fma_f32 v[64:65], v[64:65], v[20:21], v[20:21] op_sel_hi:[1,0,0]
	v_pk_fma_f32 v[66:67], v[66:67], v[20:21], v[20:21] op_sel_hi:[1,0,0]
	v_pk_fma_f32 v[68:69], v[68:69], v[20:21], v[20:21] op_sel_hi:[1,0,0]
	v_pk_fma_f32 v[70:71], v[70:71], v[20:21], v[20:21] op_sel_hi:[1,0,0]
	v_rcp_f32_e32 v64, v64
	v_rcp_f32_e32 v65, v65
	v_rcp_f32_e32 v66, v66
	v_rcp_f32_e32 v67, v67
	v_rcp_f32_e32 v68, v68
	v_rcp_f32_e32 v69, v69
	v_rcp_f32_e32 v70, v70
	v_rcp_f32_e32 v71, v71
	v_add_u32_e32 v76, 0x1b8000, v232
	v_pk_mul_f32 v[48:49], v[48:49], v[64:65]
	v_pk_mul_f32 v[50:51], v[50:51], v[66:67]
	v_pk_mul_f32 v[16:17], v[16:17], v[68:69]
	v_pk_mul_f32 v[18:19], v[18:19], v[70:71]
	v_cvt_pk_bf16_f32 v72, v48, v49
	v_cvt_pk_bf16_f32 v73, v50, v51
	v_cvt_pk_bf16_f32 v74, v16, v17
	v_cvt_pk_bf16_f32 v75, v18, v19
	global_store_dwordx4 v76, v[72:75], s[8:9] nt
	v_mul_f32_e32 v94, 0xbfb8aa3b, v231
	v_mul_f32_e32 v24, v231, v231
	v_rcp_f32_e32 v24, v24
	v_cvt_f32_i32_e32 v8, v8
	v_cvt_f32_i32_e32 v9, v9
	v_cvt_f32_i32_e32 v10, v10
	v_cvt_f32_i32_e32 v11, v11
	v_cvt_f32_i32_e32 v0, v0
	v_cvt_f32_i32_e32 v1, v1
	v_cvt_f32_i32_e32 v2, v2
	v_cvt_f32_i32_e32 v3, v3
	v_cvt_f32_i32_e32 v12, v12
	v_cvt_f32_i32_e32 v13, v13
	v_cvt_f32_i32_e32 v14, v14
	v_cvt_f32_i32_e32 v15, v15
	v_cvt_f32_i32_e32 v4, v4
	v_cvt_f32_i32_e32 v5, v5
	v_cvt_f32_i32_e32 v6, v6
	v_cvt_f32_i32_e32 v7, v7
	v_pk_mul_f32 v[80:81], v[8:9], v[94:95] op_sel_hi:[1,0]
	v_pk_mul_f32 v[82:83], v[10:11], v[94:95] op_sel_hi:[1,0]
	v_pk_mul_f32 v[84:85], v[0:1], v[94:95] op_sel_hi:[1,0]
	v_pk_mul_f32 v[86:87], v[2:3], v[94:95] op_sel_hi:[1,0]
	v_exp_f32_e32 v80, v80
	v_exp_f32_e32 v81, v81
	v_exp_f32_e32 v82, v82
	v_exp_f32_e32 v83, v83
	v_exp_f32_e32 v84, v84
	v_exp_f32_e32 v85, v85
	v_exp_f32_e32 v86, v86
	v_exp_f32_e32 v87, v87
	v_pk_mul_f32 v[8:9], v[12:13], v[8:9]
	v_pk_mul_f32 v[10:11], v[14:15], v[10:11]
	v_pk_mul_f32 v[0:1], v[4:5], v[0:1]
	v_pk_mul_f32 v[2:3], v[6:7], v[2:3]
	v_pk_fma_f32 v[80:81], v[80:81], v[24:25], v[24:25] op_sel_hi:[1,0,0]
	v_pk_fma_f32 v[82:83], v[82:83], v[24:25], v[24:25] op_sel_hi:[1,0,0]
	v_pk_fma_f32 v[84:85], v[84:85], v[24:25], v[24:25] op_sel_hi:[1,0,0]
	v_pk_fma_f32 v[86:87], v[86:87], v[24:25], v[24:25] op_sel_hi:[1,0,0]
	v_rcp_f32_e32 v80, v80
	v_rcp_f32_e32 v81, v81
	v_rcp_f32_e32 v82, v82
	v_rcp_f32_e32 v83, v83
	v_rcp_f32_e32 v84, v84
	v_rcp_f32_e32 v85, v85
	v_rcp_f32_e32 v86, v86
	v_rcp_f32_e32 v87, v87
	v_add_u32_e32 v92, 0x1e4000, v232
	v_pk_mul_f32 v[8:9], v[8:9], v[80:81]
	v_pk_mul_f32 v[10:11], v[10:11], v[82:83]
	v_pk_mul_f32 v[0:1], v[0:1], v[84:85]
	v_pk_mul_f32 v[2:3], v[2:3], v[86:87]
	v_cvt_pk_bf16_f32 v88, v8, v9
	v_cvt_pk_bf16_f32 v89, v10, v11
	v_cvt_pk_bf16_f32 v90, v0, v1
	v_cvt_pk_bf16_f32 v91, v2, v3
	global_store_dwordx4 v92, v[88:91], s[8:9] nt
	s_andn2_b64 vcc, exec, s[4:5]
	s_mov_b64 s[4:5], -1
	s_cbranch_vccnz .LBB0_749
	s_andn2_b64 vcc, exec, s[6:7]
	s_cbranch_vccnz .LBB0_748
	s_barrier
	s_branch .LBB0_748

.LBB0_1414:
	s_lshl_b32 s2, s24, 8
	s_add_i32 s2, s2, s25
	v_and_or_b32 v145, v254, 15, s2
	s_lshl_b32 s2, s22, 7
	v_ashrrev_i32_e32 v130, 1, v254
	s_or_b32 s2, s2, s49
	v_and_b32_e32 v130, -8, v130
	v_add_u32_e32 v130, s2, v130
	v_mad_u32_u24 v246, v145, s52, v130
	v_mov_b32_e32 v250, 0xb938aa3b
	v_mov_b32_e32 v251, 0xb938aa3b
	v_mov_b32_e32 v252, 0x4b000000
	v_mov_b32_e32 v253, 0x4b000000
	v_pk_mul_f32 v[146:147], v[112:113], v[250:251]
	v_pk_mul_f32 v[148:149], v[114:115], v[250:251]
	v_pk_mul_f32 v[150:151], v[116:117], v[250:251]
	v_pk_mul_f32 v[152:153], v[118:119], v[250:251]
	v_exp_f32_e32 v146, v146
	v_exp_f32_e32 v147, v147
	v_exp_f32_e32 v148, v148
	v_exp_f32_e32 v149, v149
	v_exp_f32_e32 v150, v150
	v_exp_f32_e32 v151, v151
	v_exp_f32_e32 v152, v152
	v_exp_f32_e32 v153, v153
	v_pk_mul_f32 v[112:113], v[112:113], v[120:121]
	v_pk_mul_f32 v[114:115], v[114:115], v[122:123]
	v_pk_mul_f32 v[116:117], v[116:117], v[124:125]
	v_pk_mul_f32 v[118:119], v[118:119], v[126:127]
	v_pk_fma_f32 v[146:147], v[146:147], v[252:253], v[252:253]
	v_pk_fma_f32 v[148:149], v[148:149], v[252:253], v[252:253]
	v_pk_fma_f32 v[150:151], v[150:151], v[252:253], v[252:253]
	v_pk_fma_f32 v[152:153], v[152:153], v[252:253], v[252:253]
	v_rcp_f32_e32 v146, v146
	v_rcp_f32_e32 v147, v147
	v_rcp_f32_e32 v148, v148
	v_rcp_f32_e32 v149, v149
	v_rcp_f32_e32 v150, v150
	v_rcp_f32_e32 v151, v151
	v_rcp_f32_e32 v152, v152
	v_rcp_f32_e32 v153, v153
	v_mov_b32_e32 v156, v246
	v_pk_mul_f32 v[112:113], v[112:113], v[146:147]
	v_pk_mul_f32 v[114:115], v[114:115], v[148:149]
	v_pk_mul_f32 v[116:117], v[116:117], v[150:151]
	v_pk_mul_f32 v[118:119], v[118:119], v[152:153]
	v_med3_f32 v112, v112, s51, v144
	v_med3_f32 v113, v113, s51, v144
	v_med3_f32 v114, v114, s51, v144
	v_med3_f32 v115, v115, s51, v144
	v_med3_f32 v116, v116, s51, v144
	v_med3_f32 v117, v117, s51, v144
	v_med3_f32 v118, v118, s51, v144
	v_med3_f32 v119, v119, s51, v144
	v_cvt_pk_fp8_f32 v154, v112, v113
	v_cvt_pk_fp8_f32 v155, v116, v117
	v_cvt_pk_fp8_f32 v154, v114, v115 op_sel:[0,0,1]
	v_cvt_pk_fp8_f32 v155, v118, v119 op_sel:[0,0,1]
	s_nop 0
	global_store_dwordx2 v156, v[154:155], s[10:11] nt
	v_pk_mul_f32 v[160:161], v[100:101], v[250:251]
	v_pk_mul_f32 v[162:163], v[102:103], v[250:251]
	v_pk_mul_f32 v[164:165], v[96:97], v[250:251]
	v_pk_mul_f32 v[166:167], v[98:99], v[250:251]
	v_exp_f32_e32 v160, v160
	v_exp_f32_e32 v161, v161
	v_exp_f32_e32 v162, v162
	v_exp_f32_e32 v163, v163
	v_exp_f32_e32 v164, v164
	v_exp_f32_e32 v165, v165
	v_exp_f32_e32 v166, v166
	v_exp_f32_e32 v167, v167
	v_pk_mul_f32 v[100:101], v[100:101], v[108:109]
	v_pk_mul_f32 v[102:103], v[102:103], v[110:111]
	v_pk_mul_f32 v[96:97], v[96:97], v[104:105]
	v_pk_mul_f32 v[98:99], v[98:99], v[106:107]
	v_pk_fma_f32 v[160:161], v[160:161], v[252:253], v[252:253]
	v_pk_fma_f32 v[162:163], v[162:163], v[252:253], v[252:253]
	v_pk_fma_f32 v[164:165], v[164:165], v[252:253], v[252:253]
	v_pk_fma_f32 v[166:167], v[166:167], v[252:253], v[252:253]
	v_rcp_f32_e32 v160, v160
	v_rcp_f32_e32 v161, v161
	v_rcp_f32_e32 v162, v162
	v_rcp_f32_e32 v163, v163
	v_rcp_f32_e32 v164, v164
	v_rcp_f32_e32 v165, v165
	v_rcp_f32_e32 v166, v166
	v_rcp_f32_e32 v167, v167
	v_add_u32_e32 v170, 0x1c000, v246
	v_pk_mul_f32 v[100:101], v[100:101], v[160:161]
	v_pk_mul_f32 v[102:103], v[102:103], v[162:163]
	v_pk_mul_f32 v[96:97], v[96:97], v[164:165]
	v_pk_mul_f32 v[98:99], v[98:99], v[166:167]
	v_med3_f32 v100, v100, s51, v144
	v_med3_f32 v101, v101, s51, v144
	v_med3_f32 v102, v102, s51, v144
	v_med3_f32 v103, v103, s51, v144
	v_med3_f32 v96, v96, s51, v144
	v_med3_f32 v97, v97, s51, v144
	v_med3_f32 v98, v98, s51, v144
	v_med3_f32 v99, v99, s51, v144
	v_cvt_pk_fp8_f32 v168, v100, v101
	v_cvt_pk_fp8_f32 v169, v96, v97
	v_cvt_pk_fp8_f32 v168, v102, v103 op_sel:[0,0,1]
	v_cvt_pk_fp8_f32 v169, v98, v99 op_sel:[0,0,1]
	s_nop 0
	global_store_dwordx2 v170, v[168:169], s[10:11] nt
	v_pk_mul_f32 v[146:147], v[84:85], v[250:251]
	v_pk_mul_f32 v[148:149], v[86:87], v[250:251]
	v_pk_mul_f32 v[150:151], v[80:81], v[250:251]
	v_pk_mul_f32 v[152:153], v[82:83], v[250:251]
	v_exp_f32_e32 v146, v146
	v_exp_f32_e32 v147, v147
	v_exp_f32_e32 v148, v148
	v_exp_f32_e32 v149, v149
	v_exp_f32_e32 v150, v150
	v_exp_f32_e32 v151, v151
	v_exp_f32_e32 v152, v152
	v_exp_f32_e32 v153, v153
	v_pk_mul_f32 v[84:85], v[84:85], v[92:93]
	v_pk_mul_f32 v[86:87], v[86:87], v[94:95]
	v_pk_mul_f32 v[80:81], v[80:81], v[88:89]
	v_pk_mul_f32 v[82:83], v[82:83], v[90:91]
	v_pk_fma_f32 v[146:147], v[146:147], v[252:253], v[252:253]
	v_pk_fma_f32 v[148:149], v[148:149], v[252:253], v[252:253]
	v_pk_fma_f32 v[150:151], v[150:151], v[252:253], v[252:253]
	v_pk_fma_f32 v[152:153], v[152:153], v[252:253], v[252:253]
	v_rcp_f32_e32 v146, v146
	v_rcp_f32_e32 v147, v147
	v_rcp_f32_e32 v148, v148
	v_rcp_f32_e32 v149, v149
	v_rcp_f32_e32 v150, v150
	v_rcp_f32_e32 v151, v151
	v_rcp_f32_e32 v152, v152
	v_rcp_f32_e32 v153, v153
	v_add_u32_e32 v156, 0x38000, v246
	v_pk_mul_f32 v[84:85], v[84:85], v[146:147]
	v_pk_mul_f32 v[86:87], v[86:87], v[148:149]
	v_pk_mul_f32 v[80:81], v[80:81], v[150:151]
	v_pk_mul_f32 v[82:83], v[82:83], v[152:153]
	v_med3_f32 v84, v84, s51, v144
	v_med3_f32 v85, v85, s51, v144
	v_med3_f32 v86, v86, s51, v144
	v_med3_f32 v87, v87, s51, v144
	v_med3_f32 v80, v80, s51, v144
	v_med3_f32 v81, v81, s51, v144
	v_med3_f32 v82, v82, s51, v144
	v_med3_f32 v83, v83, s51, v144
	v_cvt_pk_fp8_f32 v154, v84, v85
	v_cvt_pk_fp8_f32 v155, v80, v81
	v_cvt_pk_fp8_f32 v154, v86, v87 op_sel:[0,0,1]
	v_cvt_pk_fp8_f32 v155, v82, v83 op_sel:[0,0,1]
	s_nop 0
	global_store_dwordx2 v156, v[154:155], s[10:11] nt
	v_pk_mul_f32 v[160:161], v[60:61], v[250:251]
	v_pk_mul_f32 v[162:163], v[62:63], v[250:251]
	v_pk_mul_f32 v[164:165], v[56:57], v[250:251]
	v_pk_mul_f32 v[166:167], v[58:59], v[250:251]
	v_exp_f32_e32 v160, v160
	v_exp_f32_e32 v161, v161
	v_exp_f32_e32 v162, v162
	v_exp_f32_e32 v163, v163
	v_exp_f32_e32 v164, v164
	v_exp_f32_e32 v165, v165
	v_exp_f32_e32 v166, v166
	v_exp_f32_e32 v167, v167
	v_pk_mul_f32 v[60:61], v[60:61], v[76:77]
	v_pk_mul_f32 v[62:63], v[62:63], v[78:79]
	v_pk_mul_f32 v[56:57], v[56:57], v[72:73]
	v_pk_mul_f32 v[58:59], v[58:59], v[74:75]
	v_pk_fma_f32 v[160:161], v[160:161], v[252:253], v[252:253]
	v_pk_fma_f32 v[162:163], v[162:163], v[252:253], v[252:253]
	v_pk_fma_f32 v[164:165], v[164:165], v[252:253], v[252:253]
	v_pk_fma_f32 v[166:167], v[166:167], v[252:253], v[252:253]
	v_rcp_f32_e32 v160, v160
	v_rcp_f32_e32 v161, v161
	v_rcp_f32_e32 v162, v162
	v_rcp_f32_e32 v163, v163
	v_rcp_f32_e32 v164, v164
	v_rcp_f32_e32 v165, v165
	v_rcp_f32_e32 v166, v166
	v_rcp_f32_e32 v167, v167
	v_add_u32_e32 v170, 0x54000, v246
	v_pk_mul_f32 v[60:61], v[60:61], v[160:161]
	v_pk_mul_f32 v[62:63], v[62:63], v[162:163]
	v_pk_mul_f32 v[56:57], v[56:57], v[164:165]
	v_pk_mul_f32 v[58:59], v[58:59], v[166:167]
	v_med3_f32 v60, v60, s51, v144
	v_med3_f32 v61, v61, s51, v144
	v_med3_f32 v62, v62, s51, v144
	v_med3_f32 v63, v63, s51, v144
	v_med3_f32 v56, v56, s51, v144
	v_med3_f32 v57, v57, s51, v144
	v_med3_f32 v58, v58, s51, v144
	v_med3_f32 v59, v59, s51, v144
	v_cvt_pk_fp8_f32 v168, v60, v61
	v_cvt_pk_fp8_f32 v169, v56, v57
	v_cvt_pk_fp8_f32 v168, v62, v63 op_sel:[0,0,1]
	v_cvt_pk_fp8_f32 v169, v58, v59 op_sel:[0,0,1]
	s_nop 0
	global_store_dwordx2 v170, v[168:169], s[10:11] nt
	v_pk_mul_f32 v[146:147], v[52:53], v[250:251]
	v_pk_mul_f32 v[148:149], v[54:55], v[250:251]
	v_pk_mul_f32 v[150:151], v[48:49], v[250:251]
	v_pk_mul_f32 v[152:153], v[50:51], v[250:251]
	v_exp_f32_e32 v146, v146
	v_exp_f32_e32 v147, v147
	v_exp_f32_e32 v148, v148
	v_exp_f32_e32 v149, v149
	v_exp_f32_e32 v150, v150
	v_exp_f32_e32 v151, v151
	v_exp_f32_e32 v152, v152
	v_exp_f32_e32 v153, v153
	v_pk_mul_f32 v[52:53], v[52:53], v[68:69]
	v_pk_mul_f32 v[54:55], v[54:55], v[70:71]
	v_pk_mul_f32 v[48:49], v[48:49], v[64:65]
	v_pk_mul_f32 v[50:51], v[50:51], v[66:67]
	v_pk_fma_f32 v[146:147], v[146:147], v[252:253], v[252:253]
	v_pk_fma_f32 v[148:149], v[148:149], v[252:253], v[252:253]
	v_pk_fma_f32 v[150:151], v[150:151], v[252:253], v[252:253]
	v_pk_fma_f32 v[152:153], v[152:153], v[252:253], v[252:253]
	v_rcp_f32_e32 v146, v146
	v_rcp_f32_e32 v147, v147
	v_rcp_f32_e32 v148, v148
	v_rcp_f32_e32 v149, v149
	v_rcp_f32_e32 v150, v150
	v_rcp_f32_e32 v151, v151
	v_rcp_f32_e32 v152, v152
	v_rcp_f32_e32 v153, v153
	v_add_u32_e32 v156, 0xe0000, v246
	v_pk_mul_f32 v[52:53], v[52:53], v[146:147]
	v_pk_mul_f32 v[54:55], v[54:55], v[148:149]
	v_pk_mul_f32 v[48:49], v[48:49], v[150:151]
	v_pk_mul_f32 v[50:51], v[50:51], v[152:153]
	v_med3_f32 v52, v52, s51, v144
	v_med3_f32 v53, v53, s51, v144
	v_med3_f32 v54, v54, s51, v144
	v_med3_f32 v55, v55, s51, v144
	v_med3_f32 v48, v48, s51, v144
	v_med3_f32 v49, v49, s51, v144
	v_med3_f32 v50, v50, s51, v144
	v_med3_f32 v51, v51, s51, v144
	v_cvt_pk_fp8_f32 v154, v52, v53
	v_cvt_pk_fp8_f32 v155, v48, v49
	v_cvt_pk_fp8_f32 v154, v54, v55 op_sel:[0,0,1]
	v_cvt_pk_fp8_f32 v155, v50, v51 op_sel:[0,0,1]
	s_nop 0
	global_store_dwordx2 v156, v[154:155], s[10:11] nt
	v_pk_mul_f32 v[160:161], v[36:37], v[250:251]
	v_pk_mul_f32 v[162:163], v[38:39], v[250:251]
	v_pk_mul_f32 v[164:165], v[32:33], v[250:251]
	v_pk_mul_f32 v[166:167], v[34:35], v[250:251]
	v_exp_f32_e32 v160, v160
	v_exp_f32_e32 v161, v161
	v_exp_f32_e32 v162, v162
	v_exp_f32_e32 v163, v163
	v_exp_f32_e32 v164, v164
	v_exp_f32_e32 v165, v165
	v_exp_f32_e32 v166, v166
	v_exp_f32_e32 v167, v167
	v_pk_mul_f32 v[36:37], v[36:37], v[44:45]
	v_pk_mul_f32 v[38:39], v[38:39], v[46:47]
	v_pk_mul_f32 v[32:33], v[32:33], v[40:41]
	v_pk_mul_f32 v[34:35], v[34:35], v[42:43]
	v_pk_fma_f32 v[160:161], v[160:161], v[252:253], v[252:253]
	v_pk_fma_f32 v[162:163], v[162:163], v[252:253], v[252:253]
	v_pk_fma_f32 v[164:165], v[164:165], v[252:253], v[252:253]
	v_pk_fma_f32 v[166:167], v[166:167], v[252:253], v[252:253]
	v_rcp_f32_e32 v160, v160
	v_rcp_f32_e32 v161, v161
	v_rcp_f32_e32 v162, v162
	v_rcp_f32_e32 v163, v163
	v_rcp_f32_e32 v164, v164
	v_rcp_f32_e32 v165, v165
	v_rcp_f32_e32 v166, v166
	v_rcp_f32_e32 v167, v167
	v_add_u32_e32 v170, 0xfc000, v246
	v_pk_mul_f32 v[36:37], v[36:37], v[160:161]
	v_pk_mul_f32 v[38:39], v[38:39], v[162:163]
	v_pk_mul_f32 v[32:33], v[32:33], v[164:165]
	v_pk_mul_f32 v[34:35], v[34:35], v[166:167]
	v_med3_f32 v36, v36, s51, v144
	v_med3_f32 v37, v37, s51, v144
	v_med3_f32 v38, v38, s51, v144
	v_med3_f32 v39, v39, s51, v144
	v_med3_f32 v32, v32, s51, v144
	v_med3_f32 v33, v33, s51, v144
	v_med3_f32 v34, v34, s51, v144
	v_med3_f32 v35, v35, s51, v144
	v_cvt_pk_fp8_f32 v168, v36, v37
	v_cvt_pk_fp8_f32 v169, v32, v33
	v_cvt_pk_fp8_f32 v168, v38, v39 op_sel:[0,0,1]
	v_cvt_pk_fp8_f32 v169, v34, v35 op_sel:[0,0,1]
	s_nop 0
	global_store_dwordx2 v170, v[168:169], s[10:11] nt
	v_pk_mul_f32 v[146:147], v[20:21], v[250:251]
	v_pk_mul_f32 v[148:149], v[22:23], v[250:251]
	v_pk_mul_f32 v[150:151], v[16:17], v[250:251]
	v_pk_mul_f32 v[152:153], v[18:19], v[250:251]
	v_exp_f32_e32 v146, v146
	v_exp_f32_e32 v147, v147
	v_exp_f32_e32 v148, v148
	v_exp_f32_e32 v149, v149
	v_exp_f32_e32 v150, v150
	v_exp_f32_e32 v151, v151
	v_exp_f32_e32 v152, v152
	v_exp_f32_e32 v153, v153
	v_pk_mul_f32 v[20:21], v[20:21], v[28:29]
	v_pk_mul_f32 v[22:23], v[22:23], v[30:31]
	v_pk_mul_f32 v[16:17], v[16:17], v[24:25]
	v_pk_mul_f32 v[18:19], v[18:19], v[26:27]
	v_pk_fma_f32 v[146:147], v[146:147], v[252:253], v[252:253]
	v_pk_fma_f32 v[148:149], v[148:149], v[252:253], v[252:253]
	v_pk_fma_f32 v[150:151], v[150:151], v[252:253], v[252:253]
	v_pk_fma_f32 v[152:153], v[152:153], v[252:253], v[252:253]
	v_rcp_f32_e32 v146, v146
	v_rcp_f32_e32 v147, v147
	v_rcp_f32_e32 v148, v148
	v_rcp_f32_e32 v149, v149
	v_rcp_f32_e32 v150, v150
	v_rcp_f32_e32 v151, v151
	v_rcp_f32_e32 v152, v152
	v_rcp_f32_e32 v153, v153
	v_add_u32_e32 v156, 0x118000, v246
	v_pk_mul_f32 v[20:21], v[20:21], v[146:147]
	v_pk_mul_f32 v[22:23], v[22:23], v[148:149]
	v_pk_mul_f32 v[16:17], v[16:17], v[150:151]
	v_pk_mul_f32 v[18:19], v[18:19], v[152:153]
	v_med3_f32 v20, v20, s51, v144
	v_med3_f32 v21, v21, s51, v144
	v_med3_f32 v22, v22, s51, v144
	v_med3_f32 v23, v23, s51, v144
	v_med3_f32 v16, v16, s51, v144
	v_med3_f32 v17, v17, s51, v144
	v_med3_f32 v18, v18, s51, v144
	v_med3_f32 v19, v19, s51, v144
	v_cvt_pk_fp8_f32 v154, v20, v21
	v_cvt_pk_fp8_f32 v155, v16, v17
	v_cvt_pk_fp8_f32 v154, v22, v23 op_sel:[0,0,1]
	v_cvt_pk_fp8_f32 v155, v18, v19 op_sel:[0,0,1]
	s_nop 0
	global_store_dwordx2 v156, v[154:155], s[10:11] nt
	v_pk_mul_f32 v[160:161], v[4:5], v[250:251]
	v_pk_mul_f32 v[162:163], v[6:7], v[250:251]
	v_pk_mul_f32 v[164:165], v[0:1], v[250:251]
	v_pk_mul_f32 v[166:167], v[2:3], v[250:251]
	v_exp_f32_e32 v160, v160
	v_exp_f32_e32 v161, v161
	v_exp_f32_e32 v162, v162
	v_exp_f32_e32 v163, v163
	v_exp_f32_e32 v164, v164
	v_exp_f32_e32 v165, v165
	v_exp_f32_e32 v166, v166
	v_exp_f32_e32 v167, v167
	v_pk_mul_f32 v[4:5], v[4:5], v[12:13]
	v_pk_mul_f32 v[6:7], v[6:7], v[14:15]
	v_pk_mul_f32 v[0:1], v[0:1], v[8:9]
	v_pk_mul_f32 v[2:3], v[2:3], v[10:11]
	v_pk_fma_f32 v[160:161], v[160:161], v[252:253], v[252:253]
	v_pk_fma_f32 v[162:163], v[162:163], v[252:253], v[252:253]
	v_pk_fma_f32 v[164:165], v[164:165], v[252:253], v[252:253]
	v_pk_fma_f32 v[166:167], v[166:167], v[252:253], v[252:253]
	v_rcp_f32_e32 v160, v160
	v_rcp_f32_e32 v161, v161
	v_rcp_f32_e32 v162, v162
	v_rcp_f32_e32 v163, v163
	v_rcp_f32_e32 v164, v164
	v_rcp_f32_e32 v165, v165
	v_rcp_f32_e32 v166, v166
	v_rcp_f32_e32 v167, v167
	v_add_u32_e32 v170, 0x134000, v246
	v_pk_mul_f32 v[4:5], v[4:5], v[160:161]
	v_pk_mul_f32 v[6:7], v[6:7], v[162:163]
	v_pk_mul_f32 v[0:1], v[0:1], v[164:165]
	v_pk_mul_f32 v[2:3], v[2:3], v[166:167]
	v_med3_f32 v4, v4, s51, v144
	v_med3_f32 v5, v5, s51, v144
	v_med3_f32 v6, v6, s51, v144
	v_med3_f32 v7, v7, s51, v144
	v_med3_f32 v0, v0, s51, v144
	v_med3_f32 v1, v1, s51, v144
	v_med3_f32 v2, v2, s51, v144
	v_med3_f32 v3, v3, s51, v144
	v_cvt_pk_fp8_f32 v168, v4, v5
	v_cvt_pk_fp8_f32 v169, v0, v1
	v_cvt_pk_fp8_f32 v168, v6, v7 op_sel:[0,0,1]
	v_cvt_pk_fp8_f32 v169, v2, v3 op_sel:[0,0,1]
	s_nop 0
	global_store_dwordx2 v170, v[168:169], s[10:11] nt
	s_and_b64 vcc, exec, s[4:5]
	s_mov_b64 s[4:5], -1
	s_cbranch_vccnz .LBB0_1403
	s_andn2_b64 vcc, exec, s[8:9]
	s_cbranch_vccnz .LBB0_1402
	s_barrier
	s_branch .LBB0_1402
